# prep: W1 packing path 8 loads in one round trip (was 8 serial); slot: rank via packed key compare; gemm1 trailing-block bucketing hand-written; cache-policy sc1 on gemm1 weight loads and agg stores
# speedup vs baseline: 1.0492x; 1.0221x over previous
.LBB0_41:
	v_ashrrev_i32_e32 v2, 8, v2
	v_lshlrev_b32_e32 v4, 2, v0
	v_lshlrev_b32_e32 v8, 13, v2
	v_add_u32_e32 v4, v4, v8
	v_add_u32_e32 v5, 0x1000, v4
	v_mov_b32_e32 v10, 0
	v_mov_b32_e32 v11, 0
	v_mov_b32_e32 v12, 0
	v_mov_b32_e32 v13, 0
	v_mov_b32_e32 v14, 0
	v_mov_b32_e32 v15, 0
	v_mov_b32_e32 v16, 0
	v_mov_b32_e32 v17, 0
	s_movk_i32 s0, 0x177
	v_cmp_gt_i32_e32 vcc, s0, v2
	s_waitcnt lgkmcnt(0)
	s_and_saveexec_b64 s[0:1], vcc
	global_load_dword v10, v4, s[4:5]
	global_load_dword v11, v4, s[4:5] offset:1024
	global_load_dword v12, v4, s[4:5] offset:2048
	global_load_dword v13, v4, s[4:5] offset:3072
	global_load_dword v14, v5, s[4:5]
	global_load_dword v15, v5, s[4:5] offset:1024
	global_load_dword v16, v5, s[4:5] offset:2048
	global_load_dword v17, v5, s[4:5] offset:3072
	s_or_b64 exec, exec, s[0:1]
	v_lshlrev_b32_e32 v2, 12, v2
	v_lshl_add_u32 v2, v0, 4, v2
	s_mov_b32 s0, 0x5040100
	s_waitcnt vmcnt(0)
	v_cvt_f16_f32_e32 v10, v10
	v_cvt_f16_f32_e32 v11, v11
	v_cvt_f16_f32_e32 v12, v12
	v_cvt_f16_f32_e32 v13, v13
	v_cvt_f16_f32_e32 v14, v14
	v_cvt_f16_f32_e32 v15, v15
	v_cvt_f16_f32_e32 v16, v16
	v_cvt_f16_f32_e32 v17, v17
	v_perm_b32 v6, v11, v10, s0
	v_perm_b32 v7, v13, v12, s0
	v_perm_b32 v8, v15, v14, s0
	v_perm_b32 v9, v17, v16, s0
	global_store_dwordx4 v2, v[6:9], s[10:11]
	s_endpgm

.LBB1_39:
	s_or_b64 exec, exec, s[40:41]
	s_load_dwordx2 s[82:83], s[0:1], 0x20
	s_sub_i32 s0, 0x7530, s94
	s_min_i32 s36, s0, 0x76
	v_cmp_gt_i32_e64 s[0:1], s36, v0
	s_waitcnt lgkmcnt(0)
	s_barrier
	s_movk_i32 s37, 0x80
	v_cmp_gt_u32_e64 s[40:41], s37, v0
	s_and_saveexec_b64 s[38:39], s[40:41]
	ds_read_b32 v55, v52
	v_mov_b32_e32 v56, 0x7fffffff
	s_waitcnt lgkmcnt(0)
	v_lshl_or_b32 v55, v55, 7, v0
	v_cndmask_b32_e64 v55, v56, v55, s[0:1]
	ds_write_b32 v52, v55 offset:1440
	s_or_b64 exec, exec, s[38:39]
	s_waitcnt lgkmcnt(0)
	s_barrier
	s_and_saveexec_b64 s[92:93], s[0:1]
	s_cbranch_execz .LBB1_48
	ds_read_b32 v37, v52
	v_mov_b32_e32 v36, 0
	v_mov_b32_e32 v7, 0
	v_mov_b32_e32 v55, 0x5a0
	ds_read_b128 v[56:59], v55
	ds_read_b128 v[60:63], v55 offset:16
	s_waitcnt lgkmcnt(2)
	v_lshl_or_b32 v1, v37, 7, v0
	s_waitcnt lgkmcnt(1)
	v_cmp_lt_u32_e64 s[40:41], v56, v1
	v_cmp_lt_u32_e64 s[42:43], v57, v1
	v_cmp_lt_u32_e64 s[44:45], v58, v1
	v_cmp_lt_u32_e64 s[46:47], v59, v1
	v_addc_co_u32_e64 v36, s[40:41], 0, v36, s[40:41]
	v_addc_co_u32_e64 v36, s[42:43], 0, v36, s[42:43]
	v_addc_co_u32_e64 v36, s[44:45], 0, v36, s[44:45]
	v_addc_co_u32_e64 v36, s[46:47], 0, v36, s[46:47]
	ds_read_b128 v[56:59], v55 offset:32
	s_waitcnt lgkmcnt(1)
	v_cmp_lt_u32_e64 s[40:41], v60, v1
	v_cmp_lt_u32_e64 s[42:43], v61, v1
	v_cmp_lt_u32_e64 s[44:45], v62, v1
	v_cmp_lt_u32_e64 s[46:47], v63, v1
	v_addc_co_u32_e64 v36, s[40:41], 0, v36, s[40:41]
	v_addc_co_u32_e64 v36, s[42:43], 0, v36, s[42:43]
	v_addc_co_u32_e64 v36, s[44:45], 0, v36, s[44:45]
	v_addc_co_u32_e64 v36, s[46:47], 0, v36, s[46:47]
	ds_read_b128 v[60:63], v55 offset:48
	s_waitcnt lgkmcnt(1)
	v_cmp_lt_u32_e64 s[40:41], v56, v1
	v_cmp_lt_u32_e64 s[42:43], v57, v1
	v_cmp_lt_u32_e64 s[44:45], v58, v1
	v_cmp_lt_u32_e64 s[46:47], v59, v1
	v_addc_co_u32_e64 v36, s[40:41], 0, v36, s[40:41]
	v_addc_co_u32_e64 v36, s[42:43], 0, v36, s[42:43]
	v_addc_co_u32_e64 v36, s[44:45], 0, v36, s[44:45]
	v_addc_co_u32_e64 v36, s[46:47], 0, v36, s[46:47]
	ds_read_b128 v[56:59], v55 offset:64
	s_waitcnt lgkmcnt(1)
	v_cmp_lt_u32_e64 s[40:41], v60, v1
	v_cmp_lt_u32_e64 s[42:43], v61, v1
	v_cmp_lt_u32_e64 s[44:45], v62, v1
	v_cmp_lt_u32_e64 s[46:47], v63, v1
	v_addc_co_u32_e64 v36, s[40:41], 0, v36, s[40:41]
	v_addc_co_u32_e64 v36, s[42:43], 0, v36, s[42:43]
	v_addc_co_u32_e64 v36, s[44:45], 0, v36, s[44:45]
	v_addc_co_u32_e64 v36, s[46:47], 0, v36, s[46:47]
	ds_read_b128 v[60:63], v55 offset:80
	s_waitcnt lgkmcnt(1)
	v_cmp_lt_u32_e64 s[40:41], v56, v1
	v_cmp_lt_u32_e64 s[42:43], v57, v1
	v_cmp_lt_u32_e64 s[44:45], v58, v1
	v_cmp_lt_u32_e64 s[46:47], v59, v1
	v_addc_co_u32_e64 v36, s[40:41], 0, v36, s[40:41]
	v_addc_co_u32_e64 v36, s[42:43], 0, v36, s[42:43]
	v_addc_co_u32_e64 v36, s[44:45], 0, v36, s[44:45]
	v_addc_co_u32_e64 v36, s[46:47], 0, v36, s[46:47]
	ds_read_b128 v[56:59], v55 offset:96
	s_waitcnt lgkmcnt(1)
	v_cmp_lt_u32_e64 s[40:41], v60, v1
	v_cmp_lt_u32_e64 s[42:43], v61, v1
	v_cmp_lt_u32_e64 s[44:45], v62, v1
	v_cmp_lt_u32_e64 s[46:47], v63, v1
	v_addc_co_u32_e64 v36, s[40:41], 0, v36, s[40:41]
	v_addc_co_u32_e64 v36, s[42:43], 0, v36, s[42:43]
	v_addc_co_u32_e64 v36, s[44:45], 0, v36, s[44:45]
	v_addc_co_u32_e64 v36, s[46:47], 0, v36, s[46:47]
	ds_read_b128 v[60:63], v55 offset:112
	s_waitcnt lgkmcnt(1)
	v_cmp_lt_u32_e64 s[40:41], v56, v1
	v_cmp_lt_u32_e64 s[42:43], v57, v1
	v_cmp_lt_u32_e64 s[44:45], v58, v1
	v_cmp_lt_u32_e64 s[46:47], v59, v1
	v_addc_co_u32_e64 v36, s[40:41], 0, v36, s[40:41]
	v_addc_co_u32_e64 v36, s[42:43], 0, v36, s[42:43]
	v_addc_co_u32_e64 v36, s[44:45], 0, v36, s[44:45]
	v_addc_co_u32_e64 v36, s[46:47], 0, v36, s[46:47]
	ds_read_b128 v[56:59], v55 offset:128
	s_waitcnt lgkmcnt(1)
	v_cmp_lt_u32_e64 s[40:41], v60, v1
	v_cmp_lt_u32_e64 s[42:43], v61, v1
	v_cmp_lt_u32_e64 s[44:45], v62, v1
	v_cmp_lt_u32_e64 s[46:47], v63, v1
	v_addc_co_u32_e64 v36, s[40:41], 0, v36, s[40:41]
	v_addc_co_u32_e64 v36, s[42:43], 0, v36, s[42:43]
	v_addc_co_u32_e64 v36, s[44:45], 0, v36, s[44:45]
	v_addc_co_u32_e64 v36, s[46:47], 0, v36, s[46:47]
	ds_read_b128 v[60:63], v55 offset:144
	s_waitcnt lgkmcnt(1)
	v_cmp_lt_u32_e64 s[40:41], v56, v1
	v_cmp_lt_u32_e64 s[42:43], v57, v1
	v_cmp_lt_u32_e64 s[44:45], v58, v1
	v_cmp_lt_u32_e64 s[46:47], v59, v1
	v_addc_co_u32_e64 v36, s[40:41], 0, v36, s[40:41]
	v_addc_co_u32_e64 v36, s[42:43], 0, v36, s[42:43]
	v_addc_co_u32_e64 v36, s[44:45], 0, v36, s[44:45]
	v_addc_co_u32_e64 v36, s[46:47], 0, v36, s[46:47]
	ds_read_b128 v[56:59], v55 offset:160
	s_waitcnt lgkmcnt(1)
	v_cmp_lt_u32_e64 s[40:41], v60, v1
	v_cmp_lt_u32_e64 s[42:43], v61, v1
	v_cmp_lt_u32_e64 s[44:45], v62, v1
	v_cmp_lt_u32_e64 s[46:47], v63, v1
	v_addc_co_u32_e64 v36, s[40:41], 0, v36, s[40:41]
	v_addc_co_u32_e64 v36, s[42:43], 0, v36, s[42:43]
	v_addc_co_u32_e64 v36, s[44:45], 0, v36, s[44:45]
	v_addc_co_u32_e64 v36, s[46:47], 0, v36, s[46:47]
	ds_read_b128 v[60:63], v55 offset:176
	s_waitcnt lgkmcnt(1)
	v_cmp_lt_u32_e64 s[40:41], v56, v1
	v_cmp_lt_u32_e64 s[42:43], v57, v1
	v_cmp_lt_u32_e64 s[44:45], v58, v1
	v_cmp_lt_u32_e64 s[46:47], v59, v1
	v_addc_co_u32_e64 v36, s[40:41], 0, v36, s[40:41]
	v_addc_co_u32_e64 v36, s[42:43], 0, v36, s[42:43]
	v_addc_co_u32_e64 v36, s[44:45], 0, v36, s[44:45]
	v_addc_co_u32_e64 v36, s[46:47], 0, v36, s[46:47]
	ds_read_b128 v[56:59], v55 offset:192
	s_waitcnt lgkmcnt(1)
	v_cmp_lt_u32_e64 s[40:41], v60, v1
	v_cmp_lt_u32_e64 s[42:43], v61, v1
	v_cmp_lt_u32_e64 s[44:45], v62, v1
	v_cmp_lt_u32_e64 s[46:47], v63, v1
	v_addc_co_u32_e64 v36, s[40:41], 0, v36, s[40:41]
	v_addc_co_u32_e64 v36, s[42:43], 0, v36, s[42:43]
	v_addc_co_u32_e64 v36, s[44:45], 0, v36, s[44:45]
	v_addc_co_u32_e64 v36, s[46:47], 0, v36, s[46:47]
	ds_read_b128 v[60:63], v55 offset:208
	s_waitcnt lgkmcnt(1)
	v_cmp_lt_u32_e64 s[40:41], v56, v1
	v_cmp_lt_u32_e64 s[42:43], v57, v1
	v_cmp_lt_u32_e64 s[44:45], v58, v1
	v_cmp_lt_u32_e64 s[46:47], v59, v1
	v_addc_co_u32_e64 v36, s[40:41], 0, v36, s[40:41]
	v_addc_co_u32_e64 v36, s[42:43], 0, v36, s[42:43]
	v_addc_co_u32_e64 v36, s[44:45], 0, v36, s[44:45]
	v_addc_co_u32_e64 v36, s[46:47], 0, v36, s[46:47]
	ds_read_b128 v[56:59], v55 offset:224
	s_waitcnt lgkmcnt(1)
	v_cmp_lt_u32_e64 s[40:41], v60, v1
	v_cmp_lt_u32_e64 s[42:43], v61, v1
	v_cmp_lt_u32_e64 s[44:45], v62, v1
	v_cmp_lt_u32_e64 s[46:47], v63, v1
	v_addc_co_u32_e64 v36, s[40:41], 0, v36, s[40:41]
	v_addc_co_u32_e64 v36, s[42:43], 0, v36, s[42:43]
	v_addc_co_u32_e64 v36, s[44:45], 0, v36, s[44:45]
	v_addc_co_u32_e64 v36, s[46:47], 0, v36, s[46:47]
	ds_read_b128 v[60:63], v55 offset:240
	s_waitcnt lgkmcnt(1)
	v_cmp_lt_u32_e64 s[40:41], v56, v1
	v_cmp_lt_u32_e64 s[42:43], v57, v1
	v_cmp_lt_u32_e64 s[44:45], v58, v1
	v_cmp_lt_u32_e64 s[46:47], v59, v1
	v_addc_co_u32_e64 v36, s[40:41], 0, v36, s[40:41]
	v_addc_co_u32_e64 v36, s[42:43], 0, v36, s[42:43]
	v_addc_co_u32_e64 v36, s[44:45], 0, v36, s[44:45]
	v_addc_co_u32_e64 v36, s[46:47], 0, v36, s[46:47]
	ds_read_b128 v[56:59], v55 offset:256
	s_waitcnt lgkmcnt(1)
	v_cmp_lt_u32_e64 s[40:41], v60, v1
	v_cmp_lt_u32_e64 s[42:43], v61, v1
	v_cmp_lt_u32_e64 s[44:45], v62, v1
	v_cmp_lt_u32_e64 s[46:47], v63, v1
	v_addc_co_u32_e64 v36, s[40:41], 0, v36, s[40:41]
	v_addc_co_u32_e64 v36, s[42:43], 0, v36, s[42:43]
	v_addc_co_u32_e64 v36, s[44:45], 0, v36, s[44:45]
	v_addc_co_u32_e64 v36, s[46:47], 0, v36, s[46:47]
	ds_read_b128 v[60:63], v55 offset:272
	s_waitcnt lgkmcnt(1)
	v_cmp_lt_u32_e64 s[40:41], v56, v1
	v_cmp_lt_u32_e64 s[42:43], v57, v1
	v_cmp_lt_u32_e64 s[44:45], v58, v1
	v_cmp_lt_u32_e64 s[46:47], v59, v1
	v_addc_co_u32_e64 v36, s[40:41], 0, v36, s[40:41]
	v_addc_co_u32_e64 v36, s[42:43], 0, v36, s[42:43]
	v_addc_co_u32_e64 v36, s[44:45], 0, v36, s[44:45]
	v_addc_co_u32_e64 v36, s[46:47], 0, v36, s[46:47]
	ds_read_b128 v[56:59], v55 offset:288
	s_waitcnt lgkmcnt(1)
	v_cmp_lt_u32_e64 s[40:41], v60, v1
	v_cmp_lt_u32_e64 s[42:43], v61, v1
	v_cmp_lt_u32_e64 s[44:45], v62, v1
	v_cmp_lt_u32_e64 s[46:47], v63, v1
	v_addc_co_u32_e64 v36, s[40:41], 0, v36, s[40:41]
	v_addc_co_u32_e64 v36, s[42:43], 0, v36, s[42:43]
	v_addc_co_u32_e64 v36, s[44:45], 0, v36, s[44:45]
	v_addc_co_u32_e64 v36, s[46:47], 0, v36, s[46:47]
	ds_read_b128 v[60:63], v55 offset:304
	s_waitcnt lgkmcnt(1)
	v_cmp_lt_u32_e64 s[40:41], v56, v1
	v_cmp_lt_u32_e64 s[42:43], v57, v1
	v_cmp_lt_u32_e64 s[44:45], v58, v1
	v_cmp_lt_u32_e64 s[46:47], v59, v1
	v_addc_co_u32_e64 v36, s[40:41], 0, v36, s[40:41]
	v_addc_co_u32_e64 v36, s[42:43], 0, v36, s[42:43]
	v_addc_co_u32_e64 v36, s[44:45], 0, v36, s[44:45]
	v_addc_co_u32_e64 v36, s[46:47], 0, v36, s[46:47]
	ds_read_b128 v[56:59], v55 offset:320
	s_waitcnt lgkmcnt(1)
	v_cmp_lt_u32_e64 s[40:41], v60, v1
	v_cmp_lt_u32_e64 s[42:43], v61, v1
	v_cmp_lt_u32_e64 s[44:45], v62, v1
	v_cmp_lt_u32_e64 s[46:47], v63, v1
	v_addc_co_u32_e64 v36, s[40:41], 0, v36, s[40:41]
	v_addc_co_u32_e64 v36, s[42:43], 0, v36, s[42:43]
	v_addc_co_u32_e64 v36, s[44:45], 0, v36, s[44:45]
	v_addc_co_u32_e64 v36, s[46:47], 0, v36, s[46:47]
	ds_read_b128 v[60:63], v55 offset:336
	s_waitcnt lgkmcnt(1)
	v_cmp_lt_u32_e64 s[40:41], v56, v1
	v_cmp_lt_u32_e64 s[42:43], v57, v1
	v_cmp_lt_u32_e64 s[44:45], v58, v1
	v_cmp_lt_u32_e64 s[46:47], v59, v1
	v_addc_co_u32_e64 v36, s[40:41], 0, v36, s[40:41]
	v_addc_co_u32_e64 v36, s[42:43], 0, v36, s[42:43]
	v_addc_co_u32_e64 v36, s[44:45], 0, v36, s[44:45]
	v_addc_co_u32_e64 v36, s[46:47], 0, v36, s[46:47]
	ds_read_b128 v[56:59], v55 offset:352
	s_waitcnt lgkmcnt(1)
	v_cmp_lt_u32_e64 s[40:41], v60, v1
	v_cmp_lt_u32_e64 s[42:43], v61, v1
	v_cmp_lt_u32_e64 s[44:45], v62, v1
	v_cmp_lt_u32_e64 s[46:47], v63, v1
	v_addc_co_u32_e64 v36, s[40:41], 0, v36, s[40:41]
	v_addc_co_u32_e64 v36, s[42:43], 0, v36, s[42:43]
	v_addc_co_u32_e64 v36, s[44:45], 0, v36, s[44:45]
	v_addc_co_u32_e64 v36, s[46:47], 0, v36, s[46:47]
	ds_read_b128 v[60:63], v55 offset:368
	s_waitcnt lgkmcnt(1)
	v_cmp_lt_u32_e64 s[40:41], v56, v1
	v_cmp_lt_u32_e64 s[42:43], v57, v1
	v_cmp_lt_u32_e64 s[44:45], v58, v1
	v_cmp_lt_u32_e64 s[46:47], v59, v1
	v_addc_co_u32_e64 v36, s[40:41], 0, v36, s[40:41]
	v_addc_co_u32_e64 v36, s[42:43], 0, v36, s[42:43]
	v_addc_co_u32_e64 v36, s[44:45], 0, v36, s[44:45]
	v_addc_co_u32_e64 v36, s[46:47], 0, v36, s[46:47]
	ds_read_b128 v[56:59], v55 offset:384
	s_waitcnt lgkmcnt(1)
	v_cmp_lt_u32_e64 s[40:41], v60, v1
	v_cmp_lt_u32_e64 s[42:43], v61, v1
	v_cmp_lt_u32_e64 s[44:45], v62, v1
	v_cmp_lt_u32_e64 s[46:47], v63, v1
	v_addc_co_u32_e64 v36, s[40:41], 0, v36, s[40:41]
	v_addc_co_u32_e64 v36, s[42:43], 0, v36, s[42:43]
	v_addc_co_u32_e64 v36, s[44:45], 0, v36, s[44:45]
	v_addc_co_u32_e64 v36, s[46:47], 0, v36, s[46:47]
	ds_read_b128 v[60:63], v55 offset:400
	s_waitcnt lgkmcnt(1)
	v_cmp_lt_u32_e64 s[40:41], v56, v1
	v_cmp_lt_u32_e64 s[42:43], v57, v1
	v_cmp_lt_u32_e64 s[44:45], v58, v1
	v_cmp_lt_u32_e64 s[46:47], v59, v1
	v_addc_co_u32_e64 v36, s[40:41], 0, v36, s[40:41]
	v_addc_co_u32_e64 v36, s[42:43], 0, v36, s[42:43]
	v_addc_co_u32_e64 v36, s[44:45], 0, v36, s[44:45]
	v_addc_co_u32_e64 v36, s[46:47], 0, v36, s[46:47]
	ds_read_b128 v[56:59], v55 offset:416
	s_waitcnt lgkmcnt(1)
	v_cmp_lt_u32_e64 s[40:41], v60, v1
	v_cmp_lt_u32_e64 s[42:43], v61, v1
	v_cmp_lt_u32_e64 s[44:45], v62, v1
	v_cmp_lt_u32_e64 s[46:47], v63, v1
	v_addc_co_u32_e64 v36, s[40:41], 0, v36, s[40:41]
	v_addc_co_u32_e64 v36, s[42:43], 0, v36, s[42:43]
	v_addc_co_u32_e64 v36, s[44:45], 0, v36, s[44:45]
	v_addc_co_u32_e64 v36, s[46:47], 0, v36, s[46:47]
	ds_read_b128 v[60:63], v55 offset:432
	s_waitcnt lgkmcnt(1)
	v_cmp_lt_u32_e64 s[40:41], v56, v1
	v_cmp_lt_u32_e64 s[42:43], v57, v1
	v_cmp_lt_u32_e64 s[44:45], v58, v1
	v_cmp_lt_u32_e64 s[46:47], v59, v1
	v_addc_co_u32_e64 v36, s[40:41], 0, v36, s[40:41]
	v_addc_co_u32_e64 v36, s[42:43], 0, v36, s[42:43]
	v_addc_co_u32_e64 v36, s[44:45], 0, v36, s[44:45]
	v_addc_co_u32_e64 v36, s[46:47], 0, v36, s[46:47]
	ds_read_b128 v[56:59], v55 offset:448
	s_waitcnt lgkmcnt(1)
	v_cmp_lt_u32_e64 s[40:41], v60, v1
	v_cmp_lt_u32_e64 s[42:43], v61, v1
	v_cmp_lt_u32_e64 s[44:45], v62, v1
	v_cmp_lt_u32_e64 s[46:47], v63, v1
	v_addc_co_u32_e64 v36, s[40:41], 0, v36, s[40:41]
	v_addc_co_u32_e64 v36, s[42:43], 0, v36, s[42:43]
	v_addc_co_u32_e64 v36, s[44:45], 0, v36, s[44:45]
	v_addc_co_u32_e64 v36, s[46:47], 0, v36, s[46:47]
	ds_read_b128 v[60:63], v55 offset:464
	s_waitcnt lgkmcnt(1)
	v_cmp_lt_u32_e64 s[40:41], v56, v1
	v_cmp_lt_u32_e64 s[42:43], v57, v1
	v_cmp_lt_u32_e64 s[44:45], v58, v1
	v_cmp_lt_u32_e64 s[46:47], v59, v1
	v_addc_co_u32_e64 v36, s[40:41], 0, v36, s[40:41]
	v_addc_co_u32_e64 v36, s[42:43], 0, v36, s[42:43]
	v_addc_co_u32_e64 v36, s[44:45], 0, v36, s[44:45]
	v_addc_co_u32_e64 v36, s[46:47], 0, v36, s[46:47]
	ds_read_b128 v[56:59], v55 offset:480
	s_waitcnt lgkmcnt(1)
	v_cmp_lt_u32_e64 s[40:41], v60, v1
	v_cmp_lt_u32_e64 s[42:43], v61, v1
	v_cmp_lt_u32_e64 s[44:45], v62, v1
	v_cmp_lt_u32_e64 s[46:47], v63, v1
	v_addc_co_u32_e64 v36, s[40:41], 0, v36, s[40:41]
	v_addc_co_u32_e64 v36, s[42:43], 0, v36, s[42:43]
	v_addc_co_u32_e64 v36, s[44:45], 0, v36, s[44:45]
	v_addc_co_u32_e64 v36, s[46:47], 0, v36, s[46:47]
	ds_read_b128 v[60:63], v55 offset:496
	s_waitcnt lgkmcnt(1)
	v_cmp_lt_u32_e64 s[40:41], v56, v1
	v_cmp_lt_u32_e64 s[42:43], v57, v1
	v_cmp_lt_u32_e64 s[44:45], v58, v1
	v_cmp_lt_u32_e64 s[46:47], v59, v1
	v_addc_co_u32_e64 v36, s[40:41], 0, v36, s[40:41]
	v_addc_co_u32_e64 v36, s[42:43], 0, v36, s[42:43]
	v_addc_co_u32_e64 v36, s[44:45], 0, v36, s[44:45]
	v_addc_co_u32_e64 v36, s[46:47], 0, v36, s[46:47]
	s_waitcnt lgkmcnt(0)
	v_cmp_lt_u32_e64 s[40:41], v60, v1
	v_cmp_lt_u32_e64 s[42:43], v61, v1
	v_cmp_lt_u32_e64 s[44:45], v62, v1
	v_cmp_lt_u32_e64 s[46:47], v63, v1
	v_addc_co_u32_e64 v36, s[40:41], 0, v36, s[40:41]
	v_addc_co_u32_e64 v36, s[42:43], 0, v36, s[42:43]
	v_addc_co_u32_e64 v36, s[44:45], 0, v36, s[44:45]
	v_addc_co_u32_e64 v36, s[46:47], 0, v36, s[46:47]

	.amdhsa_kernel _Z11slot_kernelPKiS0_S0_PiS1_S1_S1_
		.amdhsa_group_segment_fixed_size 1952
		.amdhsa_private_segment_fixed_size 0
		.amdhsa_kernarg_size 56
		.amdhsa_user_sgpr_count 2
		.amdhsa_user_sgpr_dispatch_ptr 0
		.amdhsa_user_sgpr_queue_ptr 0
		.amdhsa_user_sgpr_kernarg_segment_ptr 1
		.amdhsa_user_sgpr_dispatch_id 0
		.amdhsa_user_sgpr_kernarg_preload_length 0
		.amdhsa_user_sgpr_kernarg_preload_offset 0
		.amdhsa_user_sgpr_private_segment_size 0
		.amdhsa_uses_dynamic_stack 0
		.amdhsa_enable_private_segment 0
		.amdhsa_system_sgpr_workgroup_id_x 1
		.amdhsa_system_sgpr_workgroup_id_y 0
		.amdhsa_system_sgpr_workgroup_id_z 0
		.amdhsa_system_sgpr_workgroup_info 0
		.amdhsa_system_vgpr_workitem_id 0
		.amdhsa_next_free_vgpr 65
		.amdhsa_next_free_sgpr 100
		.amdhsa_accum_offset 68
		.amdhsa_reserve_vcc 1
		.amdhsa_float_round_mode_32 0
		.amdhsa_float_round_mode_16_64 0
		.amdhsa_float_denorm_mode_32 3
		.amdhsa_float_denorm_mode_16_64 3
		.amdhsa_dx10_clamp 1
		.amdhsa_ieee_mode 1
		.amdhsa_fp16_overflow 0
		.amdhsa_tg_split 0
		.amdhsa_exception_fp_ieee_invalid_op 0
		.amdhsa_exception_fp_denorm_src 0
		.amdhsa_exception_fp_ieee_div_zero 0
		.amdhsa_exception_fp_ieee_overflow 0
		.amdhsa_exception_fp_ieee_underflow 0
		.amdhsa_exception_fp_ieee_inexact 0
		.amdhsa_exception_int_div_zero 0
	.end_amdhsa_kernel

amdhsa.kernels:
  - .agpr_count:     0
    .args:
      - .offset:         0
        .size:           248
        .value_kind:     by_value
    .group_segment_fixed_size: 0
    .kernarg_segment_align: 8
    .kernarg_segment_size: 248
    .language:       OpenCL C
    .language_version:
      - 2
      - 0
    .max_flat_workgroup_size: 256
    .name:           _Z11prep_kernel8PrepArgs
    .private_segment_fixed_size: 0
    .sgpr_count:     76
    .sgpr_spill_count: 0
    .symbol:         _Z11prep_kernel8PrepArgs.kd
    .uniform_work_group_size: 1
    .uses_dynamic_stack: false
    .vgpr_count:     29
    .vgpr_spill_count: 0
    .wavefront_size: 64
  - .agpr_count:     0
    .args:
      - .actual_access:  read_only
        .address_space:  global
        .offset:         0
        .size:           8
        .value_kind:     global_buffer
      - .actual_access:  read_only
        .address_space:  global
        .offset:         8
        .size:           8
        .value_kind:     global_buffer
      - .actual_access:  read_only
        .address_space:  global
        .offset:         16
        .size:           8
        .value_kind:     global_buffer
      - .actual_access:  write_only
        .address_space:  global
        .offset:         24
        .size:           8
        .value_kind:     global_buffer
      - .actual_access:  write_only
        .address_space:  global
        .offset:         32
        .size:           8
        .value_kind:     global_buffer
      - .actual_access:  write_only
        .address_space:  global
        .offset:         40
        .size:           8
        .value_kind:     global_buffer
      - .address_space:  global
        .offset:         48
        .size:           8
        .value_kind:     global_buffer
    .group_segment_fixed_size: 1952
    .kernarg_segment_align: 8
    .kernarg_segment_size: 56
    .language:       OpenCL C
    .language_version:
      - 2
      - 0
    .max_flat_workgroup_size: 256
    .name:           _Z11slot_kernelPKiS0_S0_PiS1_S1_S1_
    .private_segment_fixed_size: 0
    .sgpr_count:     106
    .sgpr_spill_count: 2
    .symbol:         _Z11slot_kernelPKiS0_S0_PiS1_S1_S1_.kd
    .uniform_work_group_size: 1
    .uses_dynamic_stack: false
    .vgpr_count:     65
    .vgpr_spill_count: 0
    .wavefront_size: 64
  - .agpr_count:     0
    .args:
      - .actual_access:  read_only
        .address_space:  global
        .offset:         0
        .size:           8
        .value_kind:     global_buffer
      - .actual_access:  read_only
        .address_space:  global
        .offset:         8
        .size:           8
        .value_kind:     global_buffer
      - .actual_access:  read_only
        .address_space:  global
        .offset:         16
        .size:           8
        .value_kind:     global_buffer
      - .actual_access:  read_only
        .address_space:  global
        .offset:         24
        .size:           8
        .value_kind:     global_buffer
      - .actual_access:  write_only
        .address_space:  global
        .offset:         32
        .size:           8
        .value_kind:     global_buffer
      - .actual_access:  write_only
        .address_space:  global
        .offset:         40
        .size:           8
        .value_kind:     global_buffer
    .group_segment_fixed_size: 0
    .kernarg_segment_align: 8
    .kernarg_segment_size: 48
    .language:       OpenCL C
    .language_version:
      - 2
      - 0
    .max_flat_workgroup_size: 256
    .name:           _Z13elogit_kernelPKiS0_PKfS2_PfS3_
    .private_segment_fixed_size: 0
    .sgpr_count:     18
    .sgpr_spill_count: 0
    .symbol:         _Z13elogit_kernelPKiS0_PKfS2_PfS3_.kd
    .uniform_work_group_size: 1
    .uses_dynamic_stack: false
    .vgpr_count:     28
    .vgpr_spill_count: 0
    .wavefront_size: 64
  - .agpr_count:     0
    .args:
      - .actual_access:  read_only
        .address_space:  global
        .offset:         0
        .size:           8
        .value_kind:     global_buffer
      - .actual_access:  read_only
        .address_space:  global
        .offset:         8
        .size:           8
        .value_kind:     global_buffer
      - .actual_access:  read_only
        .address_space:  global
        .offset:         16
        .size:           8
        .value_kind:     global_buffer
      - .actual_access:  read_only
        .address_space:  global
        .offset:         24
        .size:           8
        .value_kind:     global_buffer
      - .actual_access:  read_only
        .address_space:  global
        .offset:         32
        .size:           8
        .value_kind:     global_buffer
      - .actual_access:  read_only
        .address_space:  global
        .offset:         40
        .size:           8
        .value_kind:     global_buffer
      - .actual_access:  read_only
        .address_space:  global
        .offset:         48
        .size:           8
        .value_kind:     global_buffer
      - .actual_access:  read_only
        .address_space:  global
        .offset:         56
        .size:           8
        .value_kind:     global_buffer
      - .actual_access:  write_only
        .address_space:  global
        .offset:         64
        .size:           8
        .value_kind:     global_buffer
      - .actual_access:  write_only
        .address_space:  global
        .offset:         72
        .size:           8
        .value_kind:     global_buffer
      - .actual_access:  read_only
        .address_space:  global
        .offset:         80
        .size:           8
        .value_kind:     global_buffer
      - .offset:         88
        .size:           4
        .value_kind:     by_value
    .group_segment_fixed_size: 8960
    .kernarg_segment_align: 8
    .kernarg_segment_size: 92
    .language:       OpenCL C
    .language_version:
      - 2
      - 0
    .max_flat_workgroup_size: 256
    .name:           _Z10agg_kernelPKDF16_PKfS2_S2_PKiS4_S4_S2_PDF16_S5_S4_i
    .private_segment_fixed_size: 0
    .sgpr_count:     44
    .sgpr_spill_count: 0
    .symbol:         _Z10agg_kernelPKDF16_PKfS2_S2_PKiS4_S4_S2_PDF16_S5_S4_i.kd
    .uniform_work_group_size: 1
    .uses_dynamic_stack: false
    .vgpr_count:     63
    .vgpr_spill_count: 0
    .wavefront_size: 64
  - .agpr_count:     0
    .args:
      - .actual_access:  read_only
        .address_space:  global
        .offset:         0
        .size:           8
        .value_kind:     global_buffer
      - .actual_access:  read_only
        .address_space:  global
        .offset:         8
        .size:           8
        .value_kind:     global_buffer
      - .actual_access:  read_only
        .address_space:  global
        .offset:         16
        .size:           8
        .value_kind:     global_buffer
      - .actual_access:  write_only
        .address_space:  global
        .offset:         24
        .size:           8
        .value_kind:     global_buffer
    .group_segment_fixed_size: 2048
    .kernarg_segment_align: 8
    .kernarg_segment_size: 32
    .language:       OpenCL C
    .language_version:
      - 2
      - 0
    .max_flat_workgroup_size: 512
    .name:           _Z11pool_kernelPKDF16_PKiPKfPf
    .private_segment_fixed_size: 0
    .sgpr_count:     34
    .sgpr_spill_count: 0
    .symbol:         _Z11pool_kernelPKDF16_PKiPKfPf.kd
    .uniform_work_group_size: 1
    .uses_dynamic_stack: false
    .vgpr_count:     37
    .vgpr_spill_count: 0
    .wavefront_size: 64
  - .agpr_count:     0
    .args:
      - .actual_access:  write_only
        .address_space:  global
        .offset:         0
        .size:           8
        .value_kind:     global_buffer
    .group_segment_fixed_size: 0
    .kernarg_segment_align: 8
    .kernarg_segment_size: 8
    .language:       OpenCL C
    .language_version:
      - 2
      - 0
    .max_flat_workgroup_size: 512
    .name:           _Z11zero_kernelPi
    .private_segment_fixed_size: 0
    .sgpr_count:     8
    .sgpr_spill_count: 0
    .symbol:         _Z11zero_kernelPi.kd
    .uniform_work_group_size: 1
    .uses_dynamic_stack: false
    .vgpr_count:     2
    .vgpr_spill_count: 0
    .wavefront_size: 64
  - .agpr_count:     0
    .args:
      - .actual_access:  read_only
        .address_space:  global
        .offset:         0
        .size:           8
        .value_kind:     global_buffer
      - .offset:         8
        .size:           4
        .value_kind:     by_value
      - .offset:         12
        .size:           4
        .value_kind:     by_value
      - .offset:         16
        .size:           4
        .value_kind:     by_value
      - .actual_access:  read_only
        .address_space:  global
        .offset:         24
        .size:           8
        .value_kind:     global_buffer
      - .actual_access:  write_only
        .address_space:  global
        .offset:         32
        .size:           8
        .value_kind:     global_buffer
      - .actual_access:  write_only
        .address_space:  global
        .offset:         40
        .size:           8
        .value_kind:     global_buffer
      - .actual_access:  write_only
        .address_space:  global
        .offset:         48
        .size:           8
        .value_kind:     global_buffer
      - .actual_access:  read_only
        .address_space:  global
        .offset:         56
        .size:           8
        .value_kind:     global_buffer
      - .actual_access:  read_only
        .address_space:  global
        .offset:         64
        .size:           8
        .value_kind:     global_buffer
      - .offset:         72
        .size:           4
        .value_kind:     by_value
      - .offset:         76
        .size:           4
        .value_kind:     by_value
      - .offset:         80
        .size:           248
        .value_kind:     by_value
    .group_segment_fixed_size: 117136
    .kernarg_segment_align: 8
    .kernarg_segment_size: 328
    .language:       OpenCL C
    .language_version:
      - 2
      - 0
    .max_flat_workgroup_size: 512
    .name:           _Z11gemm_kernelILb1EEvPKviiiPKDF16_PDF16_PfS5_PKfS7_ii8PrepArgs
    .private_segment_fixed_size: 0
    .sgpr_count:     37
    .sgpr_spill_count: 0
    .symbol:         _Z11gemm_kernelILb1EEvPKviiiPKDF16_PDF16_PfS5_PKfS7_ii8PrepArgs.kd
    .uniform_work_group_size: 1
    .uses_dynamic_stack: false
    .vgpr_count:     233
    .vgpr_spill_count: 0
    .wavefront_size: 64
  - .agpr_count:     0
    .args:
      - .actual_access:  read_only
        .address_space:  global
        .offset:         0
        .size:           8
        .value_kind:     global_buffer
      - .offset:         8
        .size:           4
        .value_kind:     by_value
      - .offset:         12
        .size:           4
        .value_kind:     by_value
      - .offset:         16
        .size:           4
        .value_kind:     by_value
      - .actual_access:  read_only
        .address_space:  global
        .offset:         24
        .size:           8
        .value_kind:     global_buffer
      - .actual_access:  write_only
        .address_space:  global
        .offset:         32
        .size:           8
        .value_kind:     global_buffer
      - .actual_access:  write_only
        .address_space:  global
        .offset:         40
        .size:           8
        .value_kind:     global_buffer
      - .actual_access:  write_only
        .address_space:  global
        .offset:         48
        .size:           8
        .value_kind:     global_buffer
      - .actual_access:  read_only
        .address_space:  global
        .offset:         56
        .size:           8
        .value_kind:     global_buffer
      - .actual_access:  read_only
        .address_space:  global
        .offset:         64
        .size:           8
        .value_kind:     global_buffer
      - .offset:         72
        .size:           4
        .value_kind:     by_value
      - .offset:         76
        .size:           4
        .value_kind:     by_value
      - .offset:         80
        .size:           248
        .value_kind:     by_value
    .group_segment_fixed_size: 117136
    .kernarg_segment_align: 8
    .kernarg_segment_size: 328
    .language:       OpenCL C
    .language_version:
      - 2
      - 0
    .max_flat_workgroup_size: 512
    .name:           _Z11gemm_kernelILb0EEvPKviiiPKDF16_PDF16_PfS5_PKfS7_ii8PrepArgs
    .private_segment_fixed_size: 0
    .sgpr_count:     40
    .sgpr_spill_count: 0
    .symbol:         _Z11gemm_kernelILb0EEvPKviiiPKDF16_PDF16_PfS5_PKfS7_ii8PrepArgs.kd
    .uniform_work_group_size: 1
    .uses_dynamic_stack: false
    .vgpr_count:     179
    .vgpr_spill_count: 0
    .wavefront_size: 64
